# norm1 of layer 1: expert-row index quads fetched at pass start, residual row unpacked after the 32 expert-output loads are issued (one exposed round trip per row instead of two); plus router bias hois
# speedup vs baseline: 1.0037x; 1.0026x over previous
.LBB0_146:
	s_and_b64 vcc, exec, s[86:87]
	s_cbranch_vccz .Ln1_nopf
	s_add_i32 s10, s13, s18
	s_lshl_b32 s10, s10, 2
	s_ashr_i32 s11, s10, 31
	s_lshl_b64 s[10:11], s[10:11], 2
	s_add_u32 s10, s85, s10
	s_addc_u32 s11, s3, s11
	global_load_dwordx4 v[150:153], v99, s[10:11]
	global_load_dwordx4 v[154:157], v99, s[10:11] offset:16

.LBB0_148:
	s_mov_b32 s100, s6
	s_or_b32 s19, s6, s13
	s_add_i32 s6, s19, s18
	s_and_b64 vcc, exec, s[86:87]
	s_mov_b64 s[10:11], -1
	s_cbranch_vccz .LBB0_150
	s_ashr_i32 s7, s6, 31
	s_lshl_b64 s[10:11], s[6:7], 12
	v_lshl_add_u64 v[76:77], v[68:69], 0, s[10:11]
	global_load_dwordx2 v[160:161], v[76:77], off
	global_load_dwordx2 v[162:163], v[76:77], off offset:512
	global_load_dwordx2 v[164:165], v[76:77], off offset:1024
	global_load_dwordx2 v[166:167], v[76:77], off offset:1536
	global_load_dwordx2 v[168:169], v[76:77], off offset:2048
	global_load_dwordx2 v[170:171], v[76:77], off offset:2560
	global_load_dwordx2 v[172:173], v[76:77], off offset:3072
	global_load_dwordx2 v[174:175], v[76:77], off offset:3584
	s_lshl_b32 s10, s6, 2
	s_ashr_i32 s11, s10, 31
	s_lshl_b64 s[10:11], s[10:11], 2
	s_add_u32 s10, s85, s10
	s_addc_u32 s11, s3, s11
	s_cmp_lg_u32 s100, 0
	s_cbranch_scc1 .Ln1_skipw
	s_waitcnt vmcnt(8)
.Ln1_skipw:
	s_cmp_lg_u32 s100, 0
	s_cselect_b64 vcc, -1, 0
	v_cndmask_b32_e32 v56, v150, v154, vcc
	v_cndmask_b32_e32 v57, v151, v155, vcc
	v_cndmask_b32_e32 v58, v152, v156, vcc
	v_cndmask_b32_e32 v59, v153, v157, vcc
	s_mov_b64 s[10:11], 0
	v_ashrrev_i32_e32 v35, 31, v56
	v_mov_b32_e32 v34, v56
	v_lshlrev_b64 v[34:35], 11, v[34:35]
	v_lshl_add_u64 v[38:39], v[70:71], 0, v[34:35]
	global_load_dword v42, v[38:39], off nt
	global_load_dword v43, v[38:39], off offset:256 nt
	global_load_dword v44, v[38:39], off offset:512 nt
	global_load_dword v45, v[38:39], off offset:768 nt
	global_load_dword v34, v[38:39], off offset:1024 nt
	global_load_dword v35, v[38:39], off offset:1280 nt
	global_load_dword v36, v[38:39], off offset:1536 nt
	global_load_dword v37, v[38:39], off offset:1792 nt
	v_ashrrev_i32_e32 v39, 31, v57
	v_mov_b32_e32 v38, v57
	v_lshlrev_b64 v[38:39], 11, v[38:39]
	v_lshl_add_u64 v[46:47], v[70:71], 0, v[38:39]
	global_load_dword v50, v[46:47], off nt
	global_load_dword v51, v[46:47], off offset:256 nt
	global_load_dword v52, v[46:47], off offset:512 nt
	global_load_dword v53, v[46:47], off offset:768 nt
	global_load_dword v38, v[46:47], off offset:1024 nt
	global_load_dword v39, v[46:47], off offset:1280 nt
	global_load_dword v40, v[46:47], off offset:1536 nt
	global_load_dword v41, v[46:47], off offset:1792 nt
	v_ashrrev_i32_e32 v47, 31, v58
	v_mov_b32_e32 v46, v58
	v_lshlrev_b64 v[46:47], 11, v[46:47]
	v_lshl_add_u64 v[60:61], v[70:71], 0, v[46:47]
	global_load_dword v54, v[60:61], off nt
	global_load_dword v55, v[60:61], off offset:256 nt
	global_load_dword v56, v[60:61], off offset:512 nt
	global_load_dword v57, v[60:61], off offset:768 nt
	global_load_dword v46, v[60:61], off offset:1024 nt
	global_load_dword v47, v[60:61], off offset:1280 nt
	global_load_dword v48, v[60:61], off offset:1536 nt
	global_load_dword v49, v[60:61], off offset:1792 nt
	v_ashrrev_i32_e32 v61, 31, v59
	v_mov_b32_e32 v60, v59
	v_lshlrev_b64 v[58:59], 11, v[60:61]
	v_lshl_add_u64 v[112:113], v[70:71], 0, v[58:59]
	global_load_dword v62, v[112:113], off nt
	global_load_dword v63, v[112:113], off offset:256 nt
	global_load_dword v64, v[112:113], off offset:512 nt
	global_load_dword v65, v[112:113], off offset:768 nt
	global_load_dword v58, v[112:113], off offset:1024 nt
	global_load_dword v59, v[112:113], off offset:1280 nt
	global_load_dword v60, v[112:113], off offset:1536 nt
	global_load_dword v61, v[112:113], off offset:1792 nt
	s_waitcnt vmcnt(32)
	v_lshlrev_b32_e32 v108, 16, v160
	v_and_b32_e32 v109, 0xffff0000, v160
	v_lshlrev_b32_e32 v110, 16, v161
	v_and_b32_e32 v111, 0xffff0000, v161
	v_lshlrev_b32_e32 v100, 16, v164
	v_and_b32_e32 v101, 0xffff0000, v164
	v_lshlrev_b32_e32 v102, 16, v165
	v_and_b32_e32 v103, 0xffff0000, v165
	v_lshlrev_b32_e32 v104, 16, v162
	v_and_b32_e32 v105, 0xffff0000, v162
	v_lshlrev_b32_e32 v106, 16, v163
	v_and_b32_e32 v107, 0xffff0000, v163
	v_lshlrev_b32_e32 v90, 16, v168
	v_and_b32_e32 v91, 0xffff0000, v168
	v_lshlrev_b32_e32 v92, 16, v169
	v_and_b32_e32 v93, 0xffff0000, v169
	v_lshlrev_b32_e32 v86, 16, v170
	v_and_b32_e32 v87, 0xffff0000, v170
	v_lshlrev_b32_e32 v88, 16, v171
	v_and_b32_e32 v89, 0xffff0000, v171
	v_lshlrev_b32_e32 v82, 16, v172
	v_and_b32_e32 v83, 0xffff0000, v172
	v_lshlrev_b32_e32 v84, 16, v173
	v_and_b32_e32 v85, 0xffff0000, v173
	v_lshlrev_b32_e32 v94, 16, v166
	v_and_b32_e32 v95, 0xffff0000, v166
	v_lshlrev_b32_e32 v96, 16, v167
	v_and_b32_e32 v97, 0xffff0000, v167
	v_lshlrev_b32_e32 v78, 16, v174
	v_and_b32_e32 v79, 0xffff0000, v174
	v_lshlrev_b32_e32 v80, 16, v175
	v_and_b32_e32 v81, 0xffff0000, v175
	s_waitcnt vmcnt(0)
	s_nop 0
	v_cvt_pk_f32_fp8_e32 v[112:113], v36
	v_cvt_pk_f32_fp8_sdwa v[114:115], v36 src0_sel:WORD_1
	v_cvt_pk_f32_fp8_e32 v[116:117], v40
	v_cvt_pk_f32_fp8_sdwa v[118:119], v40 src0_sel:WORD_1
	v_pk_add_f32 v[112:113], v[112:113], 0 op_sel_hi:[1,0]
	v_pk_add_f32 v[114:115], v[114:115], 0 op_sel_hi:[1,0]
	v_pk_add_f32 v[112:113], v[112:113], v[116:117]
	v_pk_add_f32 v[114:115], v[114:115], v[118:119]
	v_cvt_pk_f32_fp8_e32 v[116:117], v48
	v_cvt_pk_f32_fp8_sdwa v[118:119], v48 src0_sel:WORD_1
	v_cvt_pk_f32_fp8_e32 v[120:121], v39
	v_cvt_pk_f32_fp8_sdwa v[122:123], v39 src0_sel:WORD_1
	v_pk_add_f32 v[116:117], v[112:113], v[116:117]
	v_pk_add_f32 v[112:113], v[114:115], v[118:119]
	v_cvt_pk_f32_fp8_e32 v[114:115], v60
	v_cvt_pk_f32_fp8_sdwa v[118:119], v60 src0_sel:WORD_1
	v_pk_add_f32 v[114:115], v[116:117], v[114:115]
	v_pk_add_f32 v[112:113], v[112:113], v[118:119]
	v_cvt_pk_f32_fp8_e32 v[116:117], v35
	v_cvt_pk_f32_fp8_sdwa v[118:119], v35 src0_sel:WORD_1
	v_pk_add_f32 v[116:117], v[116:117], 0 op_sel_hi:[1,0]
	v_pk_add_f32 v[118:119], v[118:119], 0 op_sel_hi:[1,0]
	v_pk_add_f32 v[116:117], v[116:117], v[120:121]
	v_pk_add_f32 v[118:119], v[118:119], v[122:123]
	v_cvt_pk_f32_fp8_e32 v[120:121], v47
	v_cvt_pk_f32_fp8_sdwa v[122:123], v47 src0_sel:WORD_1
	v_pk_add_f32 v[120:121], v[116:117], v[120:121]
	v_pk_add_f32 v[116:117], v[118:119], v[122:123]
	v_cvt_pk_f32_fp8_e32 v[118:119], v59
	v_cvt_pk_f32_fp8_sdwa v[122:123], v59 src0_sel:WORD_1
	v_pk_add_f32 v[118:119], v[120:121], v[118:119]
	v_cvt_pk_f32_fp8_e32 v[120:121], v34
	v_cvt_pk_f32_fp8_sdwa v[34:35], v34 src0_sel:WORD_1
	v_pk_add_f32 v[116:117], v[116:117], v[122:123]
	v_cvt_pk_f32_fp8_e32 v[122:123], v38
	v_cvt_pk_f32_fp8_sdwa v[38:39], v38 src0_sel:WORD_1
	v_pk_add_f32 v[120:121], v[120:121], 0 op_sel_hi:[1,0]
	v_pk_add_f32 v[34:35], v[34:35], 0 op_sel_hi:[1,0]
	s_nop 0
	v_pk_add_f32 v[34:35], v[34:35], v[38:39]
	v_pk_add_f32 v[38:39], v[120:121], v[122:123]
	v_cvt_pk_f32_fp8_e32 v[120:121], v46
	v_cvt_pk_f32_fp8_sdwa v[46:47], v46 src0_sel:WORD_1
	v_cvt_pk_f32_fp8_sdwa v[122:123], v53 src0_sel:WORD_1
	v_pk_add_f32 v[38:39], v[38:39], v[120:121]
	v_pk_add_f32 v[34:35], v[34:35], v[46:47]
	v_cvt_pk_f32_fp8_e32 v[46:47], v58
	v_cvt_pk_f32_fp8_sdwa v[58:59], v58 src0_sel:WORD_1
	v_pk_add_f32 v[120:121], v[38:39], v[46:47]
	v_pk_add_f32 v[58:59], v[34:35], v[58:59]
	v_cvt_pk_f32_fp8_e32 v[34:35], v45
	v_cvt_pk_f32_fp8_sdwa v[38:39], v45 src0_sel:WORD_1
	v_cvt_pk_f32_fp8_e32 v[46:47], v53
	v_pk_add_f32 v[34:35], v[34:35], 0 op_sel_hi:[1,0]
	v_pk_add_f32 v[38:39], v[38:39], 0 op_sel_hi:[1,0]
	v_pk_add_f32 v[34:35], v[34:35], v[46:47]
	v_pk_add_f32 v[38:39], v[38:39], v[122:123]
	v_cvt_pk_f32_fp8_e32 v[46:47], v57
	v_cvt_pk_f32_fp8_sdwa v[122:123], v57 src0_sel:WORD_1
	v_pk_add_f32 v[34:35], v[34:35], v[46:47]
	v_pk_add_f32 v[38:39], v[38:39], v[122:123]
	v_cvt_pk_f32_fp8_e32 v[122:123], v65
	v_cvt_pk_f32_fp8_sdwa v[46:47], v65 src0_sel:WORD_1
	v_pk_add_f32 v[122:123], v[34:35], v[122:123]
	v_pk_add_f32 v[46:47], v[38:39], v[46:47]
	v_cvt_pk_f32_fp8_e32 v[34:35], v44
	v_cvt_pk_f32_fp8_sdwa v[38:39], v44 src0_sel:WORD_1
	v_cvt_pk_f32_fp8_e32 v[44:45], v52
	v_cvt_pk_f32_fp8_sdwa v[52:53], v52 src0_sel:WORD_1
	v_pk_add_f32 v[34:35], v[34:35], 0 op_sel_hi:[1,0]
	v_pk_add_f32 v[38:39], v[38:39], 0 op_sel_hi:[1,0]
	v_pk_add_f32 v[34:35], v[34:35], v[44:45]
	v_pk_add_f32 v[38:39], v[38:39], v[52:53]
	v_cvt_pk_f32_fp8_e32 v[44:45], v56
	v_cvt_pk_f32_fp8_sdwa v[52:53], v56 src0_sel:WORD_1
	v_cvt_pk_f32_fp8_e32 v[56:57], v51
	v_pk_add_f32 v[34:35], v[34:35], v[44:45]
	v_pk_add_f32 v[38:39], v[38:39], v[52:53]
	v_cvt_pk_f32_fp8_e32 v[44:45], v64
	v_cvt_pk_f32_fp8_sdwa v[52:53], v64 src0_sel:WORD_1
	v_cvt_pk_f32_fp8_sdwa v[64:65], v51 src0_sel:WORD_1
	v_pk_add_f32 v[38:39], v[38:39], v[52:53]
	v_pk_add_f32 v[52:53], v[34:35], v[44:45]
	v_cvt_pk_f32_fp8_e32 v[34:35], v43
	v_cvt_pk_f32_fp8_sdwa v[44:45], v43 src0_sel:WORD_1
	v_pk_add_f32 v[34:35], v[34:35], 0 op_sel_hi:[1,0]
	v_pk_add_f32 v[44:45], v[44:45], 0 op_sel_hi:[1,0]
	v_pk_add_f32 v[34:35], v[34:35], v[56:57]
	v_cvt_pk_f32_fp8_e32 v[56:57], v55
	v_pk_add_f32 v[44:45], v[44:45], v[64:65]
	v_cvt_pk_f32_fp8_sdwa v[64:65], v55 src0_sel:WORD_1
	v_pk_add_f32 v[34:35], v[34:35], v[56:57]
	v_cvt_pk_f32_fp8_e32 v[56:57], v63
	v_pk_add_f32 v[44:45], v[44:45], v[64:65]
	v_cvt_pk_f32_fp8_sdwa v[64:65], v63 src0_sel:WORD_1
	v_pk_add_f32 v[56:57], v[34:35], v[56:57]
	v_cvt_pk_f32_fp8_e32 v[34:35], v42
	v_cvt_pk_f32_fp8_sdwa v[42:43], v42 src0_sel:WORD_1
	v_pk_add_f32 v[44:45], v[44:45], v[64:65]
	v_cvt_pk_f32_fp8_e32 v[64:65], v50
	v_cvt_pk_f32_fp8_sdwa v[50:51], v50 src0_sel:WORD_1
	v_pk_add_f32 v[42:43], v[42:43], 0 op_sel_hi:[1,0]
	v_pk_add_f32 v[34:35], v[34:35], 0 op_sel_hi:[1,0]
	v_pk_add_f32 v[42:43], v[42:43], v[50:51]
	v_cvt_pk_f32_fp8_e32 v[50:51], v54
	v_cvt_pk_f32_fp8_sdwa v[54:55], v54 src0_sel:WORD_1
	v_pk_add_f32 v[34:35], v[34:35], v[64:65]
	v_pk_add_f32 v[42:43], v[42:43], v[54:55]
	v_pk_add_f32 v[34:35], v[34:35], v[50:51]
	v_cvt_pk_f32_fp8_e32 v[50:51], v62
	v_cvt_pk_f32_fp8_sdwa v[54:55], v62 src0_sel:WORD_1
	v_pk_add_f32 v[50:51], v[34:35], v[50:51]
	v_cvt_pk_f32_fp8_e32 v[34:35], v37
	v_cvt_pk_f32_fp8_sdwa v[36:37], v37 src0_sel:WORD_1
	v_pk_add_f32 v[42:43], v[42:43], v[54:55]
	v_cvt_pk_f32_fp8_e32 v[54:55], v41
	v_cvt_pk_f32_fp8_sdwa v[40:41], v41 src0_sel:WORD_1
	v_pk_add_f32 v[36:37], v[36:37], 0 op_sel_hi:[1,0]
	v_pk_add_f32 v[34:35], v[34:35], 0 op_sel_hi:[1,0]
	v_pk_add_f32 v[36:37], v[36:37], v[40:41]
	v_cvt_pk_f32_fp8_e32 v[40:41], v49
	v_cvt_pk_f32_fp8_sdwa v[48:49], v49 src0_sel:WORD_1
	v_pk_add_f32 v[34:35], v[34:35], v[54:55]
	v_pk_add_f32 v[36:37], v[36:37], v[48:49]
	v_pk_add_f32 v[34:35], v[34:35], v[40:41]
	v_cvt_pk_f32_fp8_e32 v[40:41], v61
	v_cvt_pk_f32_fp8_sdwa v[48:49], v61 src0_sel:WORD_1
	v_pk_add_f32 v[64:65], v[34:35], v[40:41]
	v_pk_add_f32 v[62:63], v[36:37], v[48:49]
	ds_read_b128 v[34:37], v128
	s_waitcnt lgkmcnt(0)
	v_pk_mul_f32 v[34:35], v[50:51], v[34:35]
	v_pk_mul_f32 v[36:37], v[42:43], v[36:37]
	ds_read_b128 v[40:43], v128 offset:1024
	ds_read_b128 v[48:51], v128 offset:2048
	v_pk_fma_f32 v[36:37], v[36:37], s[82:83], v[110:111] op_sel_hi:[1,0,1]
	v_pk_fma_f32 v[34:35], v[34:35], s[82:83], v[108:109] op_sel_hi:[1,0,1]
	s_waitcnt lgkmcnt(1)
	v_pk_mul_f32 v[40:41], v[56:57], v[40:41]
	v_pk_mul_f32 v[42:43], v[44:45], v[42:43]
	s_waitcnt lgkmcnt(0)
	v_pk_mul_f32 v[48:49], v[52:53], v[48:49]
	v_pk_mul_f32 v[38:39], v[38:39], v[50:51]
	v_pk_fma_f32 v[44:45], v[42:43], s[82:83], v[106:107] op_sel_hi:[1,0,1]
	v_pk_fma_f32 v[42:43], v[40:41], s[82:83], v[104:105] op_sel_hi:[1,0,1]
	v_pk_fma_f32 v[40:41], v[38:39], s[82:83], v[102:103] op_sel_hi:[1,0,1]
	v_pk_fma_f32 v[38:39], v[48:49], s[82:83], v[100:101] op_sel_hi:[1,0,1]
	ds_read_b128 v[48:51], v128 offset:3072
	ds_read_b128 v[54:57], v128 offset:5120
	s_waitcnt lgkmcnt(1)
	v_pk_mul_f32 v[52:53], v[122:123], v[48:49]
	v_pk_mul_f32 v[46:47], v[46:47], v[50:51]
	s_waitcnt lgkmcnt(0)
	v_pk_mul_f32 v[54:55], v[118:119], v[54:55]
	v_pk_fma_f32 v[48:49], v[46:47], s[82:83], v[96:97] op_sel_hi:[1,0,1]
	v_pk_fma_f32 v[46:47], v[52:53], s[82:83], v[94:95] op_sel_hi:[1,0,1]
	ds_read_b128 v[50:53], v128 offset:4096
	v_pk_mul_f32 v[56:57], v[116:117], v[56:57]
	s_waitcnt lgkmcnt(0)
	v_pk_mul_f32 v[52:53], v[58:59], v[52:53]
	v_pk_fma_f32 v[60:61], v[56:57], s[82:83], v[88:89] op_sel_hi:[1,0,1]
	v_pk_fma_f32 v[58:59], v[54:55], s[82:83], v[86:87] op_sel_hi:[1,0,1]
	ds_read_b128 v[54:57], v128 offset:6144
	v_pk_mul_f32 v[50:51], v[120:121], v[50:51]
	v_pk_fma_f32 v[52:53], v[52:53], s[82:83], v[92:93] op_sel_hi:[1,0,1]
	v_pk_fma_f32 v[50:51], v[50:51], s[82:83], v[90:91] op_sel_hi:[1,0,1]
	s_waitcnt lgkmcnt(0)
	v_pk_mul_f32 v[54:55], v[114:115], v[54:55]
	v_pk_mul_f32 v[56:57], v[112:113], v[56:57]
	v_pk_fma_f32 v[54:55], v[54:55], s[82:83], v[82:83] op_sel_hi:[1,0,1]
	v_pk_fma_f32 v[56:57], v[56:57], s[82:83], v[84:85] op_sel_hi:[1,0,1]
	ds_read_b128 v[82:85], v128 offset:7168
	s_waitcnt lgkmcnt(0)
	v_pk_mul_f32 v[82:83], v[64:65], v[82:83]
	v_pk_mul_f32 v[62:63], v[62:63], v[84:85]
	s_nop 0
	v_pk_fma_f32 v[64:65], v[62:63], s[82:83], v[80:81] op_sel_hi:[1,0,1]
	v_pk_fma_f32 v[62:63], v[82:83], s[82:83], v[78:79] op_sel_hi:[1,0,1]
	v_cvt_pk_bf16_f32 v78, v34, v35
	v_cvt_pk_bf16_f32 v79, v36, v37
	global_store_dwordx2 v[76:77], v[78:79], off
	v_cvt_pk_bf16_f32 v78, v42, v43
	v_cvt_pk_bf16_f32 v79, v44, v45
	global_store_dwordx2 v[76:77], v[78:79], off offset:512
	v_cvt_pk_bf16_f32 v78, v38, v39
	v_cvt_pk_bf16_f32 v79, v40, v41
	global_store_dwordx2 v[76:77], v[78:79], off offset:1024
	v_cvt_pk_bf16_f32 v78, v46, v47
	v_cvt_pk_bf16_f32 v79, v48, v49
	global_store_dwordx2 v[76:77], v[78:79], off offset:1536
	v_cvt_pk_bf16_f32 v78, v50, v51
	v_cvt_pk_bf16_f32 v79, v52, v53
	global_store_dwordx2 v[76:77], v[78:79], off offset:2048
	v_cvt_pk_bf16_f32 v78, v58, v59
	v_cvt_pk_bf16_f32 v79, v60, v61
	global_store_dwordx2 v[76:77], v[78:79], off offset:2560
	v_cvt_pk_bf16_f32 v78, v54, v55
	v_cvt_pk_bf16_f32 v79, v56, v57
	global_store_dwordx2 v[76:77], v[78:79], off offset:3072
	v_cvt_pk_bf16_f32 v78, v62, v63
	v_cvt_pk_bf16_f32 v79, v64, v65
	global_store_dwordx2 v[76:77], v[78:79], off offset:3584
